# speedup vs baseline: 1.0771x; 1.0004x over previous
.LBB2_4:
	s_load_dwordx4 s[4:7], s[0:1], 0x0
	s_add_i32 s13, s13, -4
	v_lshrrev_b32_e32 v1, 3, v1
	v_and_b32_e32 v30, 7, v0
	s_mul_i32 s10, s8, 0x600
	s_mul_i32 s11, s9, 0x600
	s_waitcnt lgkmcnt(0)
	s_add_u32 s4, s4, s10
	s_addc_u32 s5, s5, 0
	s_add_u32 s6, s6, s11
	s_addc_u32 s7, s7, 0
	s_cmp_eq_u32 s13, 1
	s_cselect_b32 s14, s6, s4
	s_cselect_b32 s15, s7, s5
	s_cselect_b32 s16, 0xffffa000, 0
	s_mul_i32 s17, s13, 0x2a000
	s_add_u32 s4, s4, s17
	s_addc_u32 s5, s5, 0
	s_ashr_i32 s17, s16, 31
	s_add_u32 s14, s14, s16
	s_addc_u32 s15, s15, s17
	v_and_b32_e32 v31, 63, v0
	v_lshrrev_b32_e32 v32, 4, v31
	v_xor_b32_e32 v32, v32, v30
	v_lshlrev_b32_e32 v32, 4, v32
	v_mul_u32_u24_e32 v2, 0x600, v1
	v_add_u32_e32 v2, v2, v32
	v_xor_b32_e32 v3, 64, v2
	s_add_u32 s20, s4, 0x0
	s_addc_u32 s21, s5, 0
	s_add_u32 s22, s4, 0x3000
	s_addc_u32 s23, s5, 0
	s_add_u32 s24, s14, 0x6000
	s_addc_u32 s25, s15, 0
	s_add_u32 s26, s14, 0x9000
	s_addc_u32 s27, s15, 0
	s_add_u32 s28, s14, 0xc000
	s_addc_u32 s29, s15, 0
	s_add_u32 s30, s14, 0xf000
	s_addc_u32 s31, s15, 0
	s_add_u32 s32, s14, 0x12000
	s_addc_u32 s33, s15, 0
	s_add_u32 s34, s14, 0x15000
	s_addc_u32 s35, s15, 0
	s_add_u32 s36, s14, 0x18000
	s_addc_u32 s37, s15, 0
	s_add_u32 s38, s14, 0x1b000
	s_addc_u32 s39, s15, 0
	s_add_u32 s40, s14, 0x1e000
	s_addc_u32 s41, s15, 0
	s_add_u32 s42, s14, 0x21000
	s_addc_u32 s43, s15, 0
	s_add_u32 s44, s14, 0x24000
	s_addc_u32 s45, s15, 0
	s_add_u32 s46, s14, 0x27000
	s_addc_u32 s47, s15, 0
	s_mul_i32 s18, s13, 0x3800
	s_add_i32 m0, s18, 2048
	s_nop 0
	global_load_lds_dwordx4 v2, s[20:21]
	s_add_i32 m0, s18, 3072
	s_nop 0
	global_load_lds_dwordx4 v3, s[22:23]
	s_add_i32 m0, s18, 4096
	s_nop 0
	global_load_lds_dwordx4 v2, s[24:25]
	s_add_i32 m0, s18, 5120
	s_nop 0
	global_load_lds_dwordx4 v3, s[26:27]
	s_add_i32 m0, s18, 6144
	s_nop 0
	global_load_lds_dwordx4 v2, s[28:29]
	s_add_i32 m0, s18, 7168
	s_nop 0
	global_load_lds_dwordx4 v3, s[30:31]
	s_add_i32 m0, s18, 8192
	s_nop 0
	global_load_lds_dwordx4 v2, s[32:33]
	s_add_i32 m0, s18, 9216
	s_nop 0
	global_load_lds_dwordx4 v3, s[34:35]
	s_add_i32 m0, s18, 10240
	s_nop 0
	global_load_lds_dwordx4 v2, s[36:37]
	s_add_i32 m0, s18, 11264
	s_nop 0
	global_load_lds_dwordx4 v3, s[38:39]
	s_add_i32 m0, s18, 12288
	s_nop 0
	global_load_lds_dwordx4 v2, s[40:41]
	s_add_i32 m0, s18, 13312
	s_nop 0
	global_load_lds_dwordx4 v3, s[42:43]
	s_add_i32 m0, s18, 14336
	s_nop 0
	global_load_lds_dwordx4 v2, s[44:45]
	s_add_i32 m0, s18, 15360
	s_nop 0
	global_load_lds_dwordx4 v3, s[46:47]
	s_add_i32 m0, s18, 30592
	s_nop 0
	global_load_lds_dwordx4 v2, s[20:21] offset:128
	s_add_i32 m0, s18, 31616
	s_nop 0
	global_load_lds_dwordx4 v3, s[22:23] offset:128
	s_add_i32 m0, s18, 32640
	s_nop 0
	global_load_lds_dwordx4 v2, s[24:25] offset:128
	s_add_i32 m0, s18, 33664
	s_nop 0
	global_load_lds_dwordx4 v3, s[26:27] offset:128
	s_add_i32 m0, s18, 34688
	s_nop 0
	global_load_lds_dwordx4 v2, s[28:29] offset:128
	s_add_i32 m0, s18, 35712
	s_nop 0
	global_load_lds_dwordx4 v3, s[30:31] offset:128
	s_add_i32 m0, s18, 36736
	s_nop 0
	global_load_lds_dwordx4 v2, s[32:33] offset:128
	s_add_i32 m0, s18, 37760
	s_nop 0
	global_load_lds_dwordx4 v3, s[34:35] offset:128
	s_add_i32 m0, s18, 38784
	s_nop 0
	global_load_lds_dwordx4 v2, s[36:37] offset:128
	s_add_i32 m0, s18, 39808
	s_nop 0
	global_load_lds_dwordx4 v3, s[38:39] offset:128
	s_add_i32 m0, s18, 40832
	s_nop 0
	global_load_lds_dwordx4 v2, s[40:41] offset:128
	s_add_i32 m0, s18, 41856
	s_nop 0
	global_load_lds_dwordx4 v3, s[42:43] offset:128
	s_add_i32 m0, s18, 42880
	s_nop 0
	global_load_lds_dwordx4 v2, s[44:45] offset:128
	s_add_i32 m0, s18, 43904
	s_nop 0
	global_load_lds_dwordx4 v3, s[46:47] offset:128
	s_add_i32 m0, s18, 59136
	s_nop 0
	global_load_lds_dwordx4 v2, s[20:21] offset:256
	s_add_i32 m0, s18, 60160
	s_nop 0
	global_load_lds_dwordx4 v3, s[22:23] offset:256
	s_add_i32 m0, s18, 61184
	s_nop 0
	global_load_lds_dwordx4 v2, s[24:25] offset:256
	s_add_i32 m0, s18, 62208
	s_nop 0
	global_load_lds_dwordx4 v3, s[26:27] offset:256
	s_add_i32 m0, s18, 63232
	s_nop 0
	global_load_lds_dwordx4 v2, s[28:29] offset:256
	s_add_i32 m0, s18, 64256
	s_nop 0
	global_load_lds_dwordx4 v3, s[30:31] offset:256
	s_add_i32 m0, s18, 65280
	s_nop 0
	global_load_lds_dwordx4 v2, s[32:33] offset:256
	s_add_i32 m0, s18, 66304
	s_nop 0
	global_load_lds_dwordx4 v3, s[34:35] offset:256
	s_add_i32 m0, s18, 67328
	s_nop 0
	global_load_lds_dwordx4 v2, s[36:37] offset:256
	s_add_i32 m0, s18, 68352
	s_nop 0
	global_load_lds_dwordx4 v3, s[38:39] offset:256
	s_add_i32 m0, s18, 69376
	s_nop 0
	global_load_lds_dwordx4 v2, s[40:41] offset:256
	s_add_i32 m0, s18, 70400
	s_nop 0
	global_load_lds_dwordx4 v3, s[42:43] offset:256
	s_add_i32 m0, s18, 71424
	s_nop 0
	global_load_lds_dwordx4 v2, s[44:45] offset:256
	s_add_i32 m0, s18, 72448
	s_nop 0
	global_load_lds_dwordx4 v3, s[46:47] offset:256
	s_add_i32 m0, s18, 87680
	s_nop 0
	global_load_lds_dwordx4 v2, s[20:21] offset:384
	s_add_i32 m0, s18, 88704
	s_nop 0
	global_load_lds_dwordx4 v3, s[22:23] offset:384
	s_add_i32 m0, s18, 89728
	s_nop 0
	global_load_lds_dwordx4 v2, s[24:25] offset:384
	s_add_i32 m0, s18, 90752
	s_nop 0
	global_load_lds_dwordx4 v3, s[26:27] offset:384
	s_add_i32 m0, s18, 91776
	s_nop 0
	global_load_lds_dwordx4 v2, s[28:29] offset:384
	s_add_i32 m0, s18, 92800
	s_nop 0
	global_load_lds_dwordx4 v3, s[30:31] offset:384
	s_add_i32 m0, s18, 93824
	s_nop 0
	global_load_lds_dwordx4 v2, s[32:33] offset:384
	s_add_i32 m0, s18, 94848
	s_nop 0
	global_load_lds_dwordx4 v3, s[34:35] offset:384
	s_add_i32 m0, s18, 95872
	s_nop 0
	global_load_lds_dwordx4 v2, s[36:37] offset:384
	s_add_i32 m0, s18, 96896
	s_nop 0
	global_load_lds_dwordx4 v3, s[38:39] offset:384
	s_add_i32 m0, s18, 97920
	s_nop 0
	global_load_lds_dwordx4 v2, s[40:41] offset:384
	s_add_i32 m0, s18, 98944
	s_nop 0
	global_load_lds_dwordx4 v3, s[42:43] offset:384
	s_add_i32 m0, s18, 99968
	s_nop 0
	global_load_lds_dwordx4 v2, s[44:45] offset:384
	s_add_i32 m0, s18, 100992
	s_nop 0
	global_load_lds_dwordx4 v3, s[46:47] offset:384
	s_waitcnt vmcnt(42)
	s_barrier
	s_add_i32 m0, s18, 116224
	s_nop 0
	global_load_lds_dwordx4 v2, s[20:21] offset:512
	s_add_i32 m0, s18, 117248
	s_nop 0
	global_load_lds_dwordx4 v3, s[22:23] offset:512
	s_add_i32 m0, s18, 118272
	s_nop 0
	global_load_lds_dwordx4 v2, s[24:25] offset:512
	s_add_i32 m0, s18, 119296
	s_nop 0
	global_load_lds_dwordx4 v3, s[26:27] offset:512
	s_add_i32 m0, s18, 120320
	s_nop 0
	global_load_lds_dwordx4 v2, s[28:29] offset:512
	s_add_i32 m0, s18, 121344
	s_nop 0
	global_load_lds_dwordx4 v3, s[30:31] offset:512
	s_add_i32 m0, s18, 122368
	s_nop 0
	global_load_lds_dwordx4 v2, s[32:33] offset:512
	s_add_i32 m0, s18, 123392
	s_nop 0
	global_load_lds_dwordx4 v3, s[34:35] offset:512
	s_add_i32 m0, s18, 124416
	s_nop 0
	global_load_lds_dwordx4 v2, s[36:37] offset:512
	s_add_i32 m0, s18, 125440
	s_nop 0
	global_load_lds_dwordx4 v3, s[38:39] offset:512
	s_add_i32 m0, s18, 126464
	s_nop 0
	global_load_lds_dwordx4 v2, s[40:41] offset:512
	s_add_i32 m0, s18, 127488
	s_nop 0
	global_load_lds_dwordx4 v3, s[42:43] offset:512
	s_add_i32 m0, s18, 128512
	s_nop 0
	global_load_lds_dwordx4 v2, s[44:45] offset:512
	s_add_i32 m0, s18, 129536
	s_nop 0
	global_load_lds_dwordx4 v3, s[46:47] offset:512
	s_waitcnt vmcnt(42)
	s_barrier
	s_add_i32 m0, s18, 1408
	s_nop 0
	global_load_lds_dwordx4 v2, s[20:21] offset:640
	s_add_i32 m0, s18, 2432
	s_nop 0
	global_load_lds_dwordx4 v3, s[22:23] offset:640
	s_add_i32 m0, s18, 3456
	s_nop 0
	global_load_lds_dwordx4 v2, s[24:25] offset:640
	s_add_i32 m0, s18, 4480
	s_nop 0
	global_load_lds_dwordx4 v3, s[26:27] offset:640
	s_add_i32 m0, s18, 5504
	s_nop 0
	global_load_lds_dwordx4 v2, s[28:29] offset:640
	s_add_i32 m0, s18, 6528
	s_nop 0
	global_load_lds_dwordx4 v3, s[30:31] offset:640
	s_add_i32 m0, s18, 7552
	s_nop 0
	global_load_lds_dwordx4 v2, s[32:33] offset:640
	s_add_i32 m0, s18, 8576
	s_nop 0
	global_load_lds_dwordx4 v3, s[34:35] offset:640
	s_add_i32 m0, s18, 9600
	s_nop 0
	global_load_lds_dwordx4 v2, s[36:37] offset:640
	s_add_i32 m0, s18, 10624
	s_nop 0
	global_load_lds_dwordx4 v3, s[38:39] offset:640
	s_add_i32 m0, s18, 11648
	s_nop 0
	global_load_lds_dwordx4 v2, s[40:41] offset:640
	s_add_i32 m0, s18, 12672
	s_nop 0
	global_load_lds_dwordx4 v3, s[42:43] offset:640
	s_add_i32 m0, s18, 13696
	s_nop 0
	global_load_lds_dwordx4 v2, s[44:45] offset:640
	s_add_i32 m0, s18, 14720
	s_nop 0
	global_load_lds_dwordx4 v3, s[46:47] offset:640
	s_waitcnt vmcnt(42)
	s_barrier
	s_add_i32 m0, s18, 29952
	s_nop 0
	global_load_lds_dwordx4 v2, s[20:21] offset:768
	s_add_i32 m0, s18, 30976
	s_nop 0
	global_load_lds_dwordx4 v3, s[22:23] offset:768
	s_add_i32 m0, s18, 32000
	s_nop 0
	global_load_lds_dwordx4 v2, s[24:25] offset:768
	s_add_i32 m0, s18, 33024
	s_nop 0
	global_load_lds_dwordx4 v3, s[26:27] offset:768
	s_add_i32 m0, s18, 34048
	s_nop 0
	global_load_lds_dwordx4 v2, s[28:29] offset:768
	s_add_i32 m0, s18, 35072
	s_nop 0
	global_load_lds_dwordx4 v3, s[30:31] offset:768
	s_add_i32 m0, s18, 36096
	s_nop 0
	global_load_lds_dwordx4 v2, s[32:33] offset:768
	s_add_i32 m0, s18, 37120
	s_nop 0
	global_load_lds_dwordx4 v3, s[34:35] offset:768
	s_add_i32 m0, s18, 38144
	s_nop 0
	global_load_lds_dwordx4 v2, s[36:37] offset:768
	s_add_i32 m0, s18, 39168
	s_nop 0
	global_load_lds_dwordx4 v3, s[38:39] offset:768
	s_add_i32 m0, s18, 40192
	s_nop 0
	global_load_lds_dwordx4 v2, s[40:41] offset:768
	s_add_i32 m0, s18, 41216
	s_nop 0
	global_load_lds_dwordx4 v3, s[42:43] offset:768
	s_add_i32 m0, s18, 42240
	s_nop 0
	global_load_lds_dwordx4 v2, s[44:45] offset:768
	s_add_i32 m0, s18, 43264
	s_nop 0
	global_load_lds_dwordx4 v3, s[46:47] offset:768
	s_waitcnt vmcnt(42)
	s_barrier
	s_add_i32 m0, s18, 58496
	s_nop 0
	global_load_lds_dwordx4 v2, s[20:21] offset:896
	s_add_i32 m0, s18, 59520
	s_nop 0
	global_load_lds_dwordx4 v3, s[22:23] offset:896
	s_add_i32 m0, s18, 60544
	s_nop 0
	global_load_lds_dwordx4 v2, s[24:25] offset:896
	s_add_i32 m0, s18, 61568
	s_nop 0
	global_load_lds_dwordx4 v3, s[26:27] offset:896
	s_add_i32 m0, s18, 62592
	s_nop 0
	global_load_lds_dwordx4 v2, s[28:29] offset:896
	s_add_i32 m0, s18, 63616
	s_nop 0
	global_load_lds_dwordx4 v3, s[30:31] offset:896
	s_add_i32 m0, s18, 64640
	s_nop 0
	global_load_lds_dwordx4 v2, s[32:33] offset:896
	s_add_i32 m0, s18, 65664
	s_nop 0
	global_load_lds_dwordx4 v3, s[34:35] offset:896
	s_add_i32 m0, s18, 66688
	s_nop 0
	global_load_lds_dwordx4 v2, s[36:37] offset:896
	s_add_i32 m0, s18, 67712
	s_nop 0
	global_load_lds_dwordx4 v3, s[38:39] offset:896
	s_add_i32 m0, s18, 68736
	s_nop 0
	global_load_lds_dwordx4 v2, s[40:41] offset:896
	s_add_i32 m0, s18, 69760
	s_nop 0
	global_load_lds_dwordx4 v3, s[42:43] offset:896
	s_add_i32 m0, s18, 70784
	s_nop 0
	global_load_lds_dwordx4 v2, s[44:45] offset:896
	s_add_i32 m0, s18, 71808
	s_nop 0
	global_load_lds_dwordx4 v3, s[46:47] offset:896
	s_waitcnt vmcnt(42)
	s_barrier
	s_add_i32 m0, s18, 87040
	s_nop 0
	global_load_lds_dwordx4 v2, s[20:21] offset:1024
	s_add_i32 m0, s18, 88064
	s_nop 0
	global_load_lds_dwordx4 v3, s[22:23] offset:1024
	s_add_i32 m0, s18, 89088
	s_nop 0
	global_load_lds_dwordx4 v2, s[24:25] offset:1024
	s_add_i32 m0, s18, 90112
	s_nop 0
	global_load_lds_dwordx4 v3, s[26:27] offset:1024
	s_add_i32 m0, s18, 91136
	s_nop 0
	global_load_lds_dwordx4 v2, s[28:29] offset:1024
	s_add_i32 m0, s18, 92160
	s_nop 0
	global_load_lds_dwordx4 v3, s[30:31] offset:1024
	s_add_i32 m0, s18, 93184
	s_nop 0
	global_load_lds_dwordx4 v2, s[32:33] offset:1024
	s_add_i32 m0, s18, 94208
	s_nop 0
	global_load_lds_dwordx4 v3, s[34:35] offset:1024
	s_add_i32 m0, s18, 95232
	s_nop 0
	global_load_lds_dwordx4 v2, s[36:37] offset:1024
	s_add_i32 m0, s18, 96256
	s_nop 0
	global_load_lds_dwordx4 v3, s[38:39] offset:1024
	s_add_i32 m0, s18, 97280
	s_nop 0
	global_load_lds_dwordx4 v2, s[40:41] offset:1024
	s_add_i32 m0, s18, 98304
	s_nop 0
	global_load_lds_dwordx4 v3, s[42:43] offset:1024
	s_add_i32 m0, s18, 99328
	s_nop 0
	global_load_lds_dwordx4 v2, s[44:45] offset:1024
	s_add_i32 m0, s18, 100352
	s_nop 0
	global_load_lds_dwordx4 v3, s[46:47] offset:1024
	s_waitcnt vmcnt(42)
	s_barrier
	s_add_i32 m0, s18, 115584
	s_nop 0
	global_load_lds_dwordx4 v2, s[20:21] offset:1152
	s_add_i32 m0, s18, 116608
	s_nop 0
	global_load_lds_dwordx4 v3, s[22:23] offset:1152
	s_add_i32 m0, s18, 117632
	s_nop 0
	global_load_lds_dwordx4 v2, s[24:25] offset:1152
	s_add_i32 m0, s18, 118656
	s_nop 0
	global_load_lds_dwordx4 v3, s[26:27] offset:1152
	s_add_i32 m0, s18, 119680
	s_nop 0
	global_load_lds_dwordx4 v2, s[28:29] offset:1152
	s_add_i32 m0, s18, 120704
	s_nop 0
	global_load_lds_dwordx4 v3, s[30:31] offset:1152
	s_add_i32 m0, s18, 121728
	s_nop 0
	global_load_lds_dwordx4 v2, s[32:33] offset:1152
	s_add_i32 m0, s18, 122752
	s_nop 0
	global_load_lds_dwordx4 v3, s[34:35] offset:1152
	s_add_i32 m0, s18, 123776
	s_nop 0
	global_load_lds_dwordx4 v2, s[36:37] offset:1152
	s_add_i32 m0, s18, 124800
	s_nop 0
	global_load_lds_dwordx4 v3, s[38:39] offset:1152
	s_add_i32 m0, s18, 125824
	s_nop 0
	global_load_lds_dwordx4 v2, s[40:41] offset:1152
	s_add_i32 m0, s18, 126848
	s_nop 0
	global_load_lds_dwordx4 v3, s[42:43] offset:1152
	s_add_i32 m0, s18, 127872
	s_nop 0
	global_load_lds_dwordx4 v2, s[44:45] offset:1152
	s_add_i32 m0, s18, 128896
	s_nop 0
	global_load_lds_dwordx4 v3, s[46:47] offset:1152
	s_waitcnt vmcnt(42)
	s_barrier
	s_add_i32 m0, s18, 768
	s_nop 0
	global_load_lds_dwordx4 v2, s[20:21] offset:1280
	s_add_i32 m0, s18, 1792
	s_nop 0
	global_load_lds_dwordx4 v3, s[22:23] offset:1280
	s_add_i32 m0, s18, 2816
	s_nop 0
	global_load_lds_dwordx4 v2, s[24:25] offset:1280
	s_add_i32 m0, s18, 3840
	s_nop 0
	global_load_lds_dwordx4 v3, s[26:27] offset:1280
	s_add_i32 m0, s18, 4864
	s_nop 0
	global_load_lds_dwordx4 v2, s[28:29] offset:1280
	s_add_i32 m0, s18, 5888
	s_nop 0
	global_load_lds_dwordx4 v3, s[30:31] offset:1280
	s_add_i32 m0, s18, 6912
	s_nop 0
	global_load_lds_dwordx4 v2, s[32:33] offset:1280
	s_add_i32 m0, s18, 7936
	s_nop 0
	global_load_lds_dwordx4 v3, s[34:35] offset:1280
	s_add_i32 m0, s18, 8960
	s_nop 0
	global_load_lds_dwordx4 v2, s[36:37] offset:1280
	s_add_i32 m0, s18, 9984
	s_nop 0
	global_load_lds_dwordx4 v3, s[38:39] offset:1280
	s_add_i32 m0, s18, 11008
	s_nop 0
	global_load_lds_dwordx4 v2, s[40:41] offset:1280
	s_add_i32 m0, s18, 12032
	s_nop 0
	global_load_lds_dwordx4 v3, s[42:43] offset:1280
	s_add_i32 m0, s18, 13056
	s_nop 0
	global_load_lds_dwordx4 v2, s[44:45] offset:1280
	s_add_i32 m0, s18, 14080
	s_nop 0
	global_load_lds_dwordx4 v3, s[46:47] offset:1280
	s_waitcnt vmcnt(42)
	s_barrier
	s_add_i32 m0, s18, 29312
	s_nop 0
	global_load_lds_dwordx4 v2, s[20:21] offset:1408
	s_add_i32 m0, s18, 30336
	s_nop 0
	global_load_lds_dwordx4 v3, s[22:23] offset:1408
	s_add_i32 m0, s18, 31360
	s_nop 0
	global_load_lds_dwordx4 v2, s[24:25] offset:1408
	s_add_i32 m0, s18, 32384
	s_nop 0
	global_load_lds_dwordx4 v3, s[26:27] offset:1408
	s_add_i32 m0, s18, 33408
	s_nop 0
	global_load_lds_dwordx4 v2, s[28:29] offset:1408
	s_add_i32 m0, s18, 34432
	s_nop 0
	global_load_lds_dwordx4 v3, s[30:31] offset:1408
	s_add_i32 m0, s18, 35456
	s_nop 0
	global_load_lds_dwordx4 v2, s[32:33] offset:1408
	s_add_i32 m0, s18, 36480
	s_nop 0
	global_load_lds_dwordx4 v3, s[34:35] offset:1408
	s_add_i32 m0, s18, 37504
	s_nop 0
	global_load_lds_dwordx4 v2, s[36:37] offset:1408
	s_add_i32 m0, s18, 38528
	s_nop 0
	global_load_lds_dwordx4 v3, s[38:39] offset:1408
	s_add_i32 m0, s18, 39552
	s_nop 0
	global_load_lds_dwordx4 v2, s[40:41] offset:1408
	s_add_i32 m0, s18, 40576
	s_nop 0
	global_load_lds_dwordx4 v3, s[42:43] offset:1408
	s_add_i32 m0, s18, 41600
	s_nop 0
	global_load_lds_dwordx4 v2, s[44:45] offset:1408
	s_add_i32 m0, s18, 42624
	s_nop 0
	global_load_lds_dwordx4 v3, s[46:47] offset:1408
	s_waitcnt vmcnt(42)
	s_barrier
	s_waitcnt vmcnt(28)
	s_barrier
	s_waitcnt vmcnt(14)
	s_barrier
	s_waitcnt vmcnt(0)
	s_barrier
	s_endpgm
